# speedup vs baseline: 1.0386x; 1.0013x over previous
.Lsc3_loop:
	s_waitcnt lgkmcnt(0)
	ds_read_b128 v[196:199], v57 offset:64
	ds_read_b128 v[200:203], v57 offset:80
	ds_read_b128 v[204:207], v57 offset:96
	ds_read_b128 v[208:211], v57 offset:112
	ds_read_b128 v[212:215], v57 offset:4160
	ds_read_b128 v[216:219], v57 offset:4176
	ds_read_b128 v[220:223], v57 offset:4192
	ds_read_b128 v[224:227], v57 offset:4208
	v_cvt_f32_f16_e32 v46, v181
	v_cvt_f32_f16_e32 v53, v52
	ds_read_u16 v52, v19 offset:528
	v_pk_mul_f32 v[94:95], v[94:95], v[20:21]
	v_pk_mul_f32 v[20:21], v[46:47], v[14:15] op_sel_hi:[0,1]
	v_mul_f32_e32 v55, 0xbfb8aa3b, v53
	v_pk_mul_f32 v[102:103], v[102:103], v[22:23]
	v_exp_f32_e32 v20, v20
	v_pk_mul_f32 v[22:23], v[46:47], v[16:17] op_sel_hi:[0,1]
	v_pk_fma_f32 v[94:95], v[44:45], v[116:117], v[94:95] op_sel_hi:[0,1,1]
	v_exp_f32_e32 v21, v21
	v_pk_mul_f32 v[48:49], v[94:95], v[132:133]
	v_pk_mul_f32 v[88:89], v[88:89], v[24:25]
	v_exp_f32_e32 v22, v22
	v_pk_mul_f32 v[24:25], v[46:47], v[10:11] op_sel_hi:[0,1]
	v_pk_fma_f32 v[102:103], v[44:45], v[118:119], v[102:103] op_sel_hi:[0,1,1]
	v_exp_f32_e32 v23, v23
	v_pk_fma_f32 v[48:49], v[102:103], v[134:135], v[48:49]
	v_exp_f32_e32 v55, v55
	v_pk_mul_f32 v[96:97], v[96:97], v[26:27]
	v_exp_f32_e32 v24, v24
	v_pk_mul_f32 v[26:27], v[46:47], v[12:13] op_sel_hi:[0,1]
	v_pk_fma_f32 v[88:89], v[44:45], v[120:121], v[88:89] op_sel_hi:[0,1,1]
	v_exp_f32_e32 v25, v25
	v_pk_fma_f32 v[48:49], v[88:89], v[136:137], v[48:49]
	v_pk_mul_f32 v[90:91], v[90:91], v[28:29]
	v_exp_f32_e32 v26, v26
	v_pk_mul_f32 v[28:29], v[46:47], v[6:7] op_sel_hi:[0,1]
	v_pk_fma_f32 v[96:97], v[44:45], v[122:123], v[96:97] op_sel_hi:[0,1,1]
	v_exp_f32_e32 v27, v27
	v_pk_fma_f32 v[48:49], v[96:97], v[138:139], v[48:49]
	v_add_f32_e32 v55, 1.0, v55
	v_pk_mul_f32 v[92:93], v[92:93], v[30:31]
	v_exp_f32_e32 v28, v28
	v_pk_mul_f32 v[30:31], v[46:47], v[8:9] op_sel_hi:[0,1]
	v_pk_fma_f32 v[90:91], v[44:45], v[124:125], v[90:91] op_sel_hi:[0,1,1]
	v_exp_f32_e32 v29, v29
	v_pk_fma_f32 v[48:49], v[90:91], v[140:141], v[48:49]
	v_pk_mul_f32 v[98:99], v[98:99], v[32:33]
	v_exp_f32_e32 v30, v30
	v_pk_mul_f32 v[32:33], v[46:47], v[2:3] op_sel_hi:[0,1]
	v_pk_fma_f32 v[92:93], v[44:45], v[126:127], v[92:93] op_sel_hi:[0,1,1]
	v_exp_f32_e32 v31, v31
	v_pk_fma_f32 v[48:49], v[92:93], v[142:143], v[48:49]
	v_rcp_f32_e32 v55, v55
	v_pk_mul_f32 v[100:101], v[100:101], v[34:35]
	v_exp_f32_e32 v32, v32
	v_pk_mul_f32 v[34:35], v[46:47], v[4:5] op_sel_hi:[0,1]
	v_pk_fma_f32 v[98:99], v[44:45], v[128:129], v[98:99] op_sel_hi:[0,1,1]
	v_exp_f32_e32 v33, v33
	v_pk_fma_f32 v[48:49], v[98:99], v[144:145], v[48:49]
	v_exp_f32_e32 v34, v34
	v_pk_fma_f32 v[100:101], v[44:45], v[130:131], v[100:101] op_sel_hi:[0,1,1]
	v_exp_f32_e32 v35, v35
	v_pk_fma_f32 v[48:49], v[100:101], v[146:147], v[48:49]
	v_add_f32_e32 v54, v48, v49
	v_fma_mix_f32 v54, v87, v180, v54 op_sel:[0,1,0] op_sel_hi:[0,1,0]
	v_mul_f32_e32 v54, v54, v53
	v_fma_mix_f32 v44, v181, v181, 0 op_sel:[0,1,0] op_sel_hi:[1,1,0]
	v_fma_mixlo_f16 v56, v54, v55, 0
	ds_write_b16 v19, v56
	s_waitcnt lgkmcnt(1)
	ds_read_b128 v[116:119], v57 offset:128
	ds_read_b128 v[120:123], v57 offset:144
	ds_read_b128 v[124:127], v57 offset:160
	ds_read_b128 v[128:131], v57 offset:176
	ds_read_b128 v[132:135], v57 offset:4224
	ds_read_b128 v[136:139], v57 offset:4240
	ds_read_b128 v[140:143], v57 offset:4256
	ds_read_b128 v[144:147], v57 offset:4272
	v_cvt_f32_f16_e32 v46, v182
	v_cvt_f32_f16_e32 v53, v52
	ds_read_u16 v52, v19 offset:1056
	v_pk_mul_f32 v[94:95], v[94:95], v[20:21]
	v_pk_mul_f32 v[20:21], v[46:47], v[14:15] op_sel_hi:[0,1]
	v_mul_f32_e32 v55, 0xbfb8aa3b, v53
	v_pk_mul_f32 v[102:103], v[102:103], v[22:23]
	v_exp_f32_e32 v20, v20
	v_pk_mul_f32 v[22:23], v[46:47], v[16:17] op_sel_hi:[0,1]
	v_pk_fma_f32 v[94:95], v[44:45], v[196:197], v[94:95] op_sel_hi:[0,1,1]
	v_exp_f32_e32 v21, v21
	v_pk_mul_f32 v[48:49], v[94:95], v[212:213]
	v_pk_mul_f32 v[88:89], v[88:89], v[24:25]
	v_exp_f32_e32 v22, v22
	v_pk_mul_f32 v[24:25], v[46:47], v[10:11] op_sel_hi:[0,1]
	v_pk_fma_f32 v[102:103], v[44:45], v[198:199], v[102:103] op_sel_hi:[0,1,1]
	v_exp_f32_e32 v23, v23
	v_pk_fma_f32 v[48:49], v[102:103], v[214:215], v[48:49]
	v_exp_f32_e32 v55, v55
	v_pk_mul_f32 v[96:97], v[96:97], v[26:27]
	v_exp_f32_e32 v24, v24
	v_pk_mul_f32 v[26:27], v[46:47], v[12:13] op_sel_hi:[0,1]
	v_pk_fma_f32 v[88:89], v[44:45], v[200:201], v[88:89] op_sel_hi:[0,1,1]
	v_exp_f32_e32 v25, v25
	v_pk_fma_f32 v[48:49], v[88:89], v[216:217], v[48:49]
	v_pk_mul_f32 v[90:91], v[90:91], v[28:29]
	v_exp_f32_e32 v26, v26
	v_pk_mul_f32 v[28:29], v[46:47], v[6:7] op_sel_hi:[0,1]
	v_pk_fma_f32 v[96:97], v[44:45], v[202:203], v[96:97] op_sel_hi:[0,1,1]
	v_exp_f32_e32 v27, v27
	v_pk_fma_f32 v[48:49], v[96:97], v[218:219], v[48:49]
	v_add_f32_e32 v55, 1.0, v55
	v_pk_mul_f32 v[92:93], v[92:93], v[30:31]
	v_exp_f32_e32 v28, v28
	v_pk_mul_f32 v[30:31], v[46:47], v[8:9] op_sel_hi:[0,1]
	v_pk_fma_f32 v[90:91], v[44:45], v[204:205], v[90:91] op_sel_hi:[0,1,1]
	v_exp_f32_e32 v29, v29
	v_pk_fma_f32 v[48:49], v[90:91], v[220:221], v[48:49]
	v_pk_mul_f32 v[98:99], v[98:99], v[32:33]
	v_exp_f32_e32 v30, v30
	v_pk_mul_f32 v[32:33], v[46:47], v[2:3] op_sel_hi:[0,1]
	v_pk_fma_f32 v[92:93], v[44:45], v[206:207], v[92:93] op_sel_hi:[0,1,1]
	v_exp_f32_e32 v31, v31
	v_pk_fma_f32 v[48:49], v[92:93], v[222:223], v[48:49]
	v_rcp_f32_e32 v55, v55
	v_pk_mul_f32 v[100:101], v[100:101], v[34:35]
	v_exp_f32_e32 v32, v32
	v_pk_mul_f32 v[34:35], v[46:47], v[4:5] op_sel_hi:[0,1]
	v_pk_fma_f32 v[98:99], v[44:45], v[208:209], v[98:99] op_sel_hi:[0,1,1]
	v_exp_f32_e32 v33, v33
	v_pk_fma_f32 v[48:49], v[98:99], v[224:225], v[48:49]
	v_exp_f32_e32 v34, v34
	v_pk_fma_f32 v[100:101], v[44:45], v[210:211], v[100:101] op_sel_hi:[0,1,1]
	v_exp_f32_e32 v35, v35
	v_pk_fma_f32 v[48:49], v[100:101], v[226:227], v[48:49]
	v_add_f32_e32 v54, v48, v49
	v_fma_mix_f32 v54, v87, v181, v54 op_sel:[0,1,0] op_sel_hi:[0,1,0]
	v_mul_f32_e32 v54, v54, v53
	v_fma_mix_f32 v44, v182, v182, 0 op_sel:[0,1,0] op_sel_hi:[1,1,0]
	v_fma_mixlo_f16 v56, v54, v55, 0
	ds_write_b16 v19, v56 offset:528
	s_waitcnt lgkmcnt(1)
	ds_read_b128 v[196:199], v57 offset:192
	ds_read_b128 v[200:203], v57 offset:208
	ds_read_b128 v[204:207], v57 offset:224
	ds_read_b128 v[208:211], v57 offset:240
	ds_read_b128 v[212:215], v57 offset:4288
	ds_read_b128 v[216:219], v57 offset:4304
	ds_read_b128 v[220:223], v57 offset:4320
	ds_read_b128 v[224:227], v57 offset:4336
	v_cvt_f32_f16_e32 v46, v183
	v_cvt_f32_f16_e32 v53, v52
	ds_read_u16 v52, v19 offset:1584
	v_pk_mul_f32 v[94:95], v[94:95], v[20:21]
	v_pk_mul_f32 v[20:21], v[46:47], v[14:15] op_sel_hi:[0,1]
	v_mul_f32_e32 v55, 0xbfb8aa3b, v53
	v_pk_mul_f32 v[102:103], v[102:103], v[22:23]
	v_exp_f32_e32 v20, v20
	v_pk_mul_f32 v[22:23], v[46:47], v[16:17] op_sel_hi:[0,1]
	v_pk_fma_f32 v[94:95], v[44:45], v[116:117], v[94:95] op_sel_hi:[0,1,1]
	v_exp_f32_e32 v21, v21
	v_pk_mul_f32 v[48:49], v[94:95], v[132:133]
	v_pk_mul_f32 v[88:89], v[88:89], v[24:25]
	v_exp_f32_e32 v22, v22
	v_pk_mul_f32 v[24:25], v[46:47], v[10:11] op_sel_hi:[0,1]
	v_pk_fma_f32 v[102:103], v[44:45], v[118:119], v[102:103] op_sel_hi:[0,1,1]
	v_exp_f32_e32 v23, v23
	v_pk_fma_f32 v[48:49], v[102:103], v[134:135], v[48:49]
	v_exp_f32_e32 v55, v55
	v_pk_mul_f32 v[96:97], v[96:97], v[26:27]
	v_exp_f32_e32 v24, v24
	v_pk_mul_f32 v[26:27], v[46:47], v[12:13] op_sel_hi:[0,1]
	v_pk_fma_f32 v[88:89], v[44:45], v[120:121], v[88:89] op_sel_hi:[0,1,1]
	v_exp_f32_e32 v25, v25
	v_pk_fma_f32 v[48:49], v[88:89], v[136:137], v[48:49]
	v_pk_mul_f32 v[90:91], v[90:91], v[28:29]
	v_exp_f32_e32 v26, v26
	v_pk_mul_f32 v[28:29], v[46:47], v[6:7] op_sel_hi:[0,1]
	v_pk_fma_f32 v[96:97], v[44:45], v[122:123], v[96:97] op_sel_hi:[0,1,1]
	v_exp_f32_e32 v27, v27
	v_pk_fma_f32 v[48:49], v[96:97], v[138:139], v[48:49]
	v_add_f32_e32 v55, 1.0, v55
	v_pk_mul_f32 v[92:93], v[92:93], v[30:31]
	v_exp_f32_e32 v28, v28
	v_pk_mul_f32 v[30:31], v[46:47], v[8:9] op_sel_hi:[0,1]
	v_pk_fma_f32 v[90:91], v[44:45], v[124:125], v[90:91] op_sel_hi:[0,1,1]
	v_exp_f32_e32 v29, v29
	v_pk_fma_f32 v[48:49], v[90:91], v[140:141], v[48:49]
	v_pk_mul_f32 v[98:99], v[98:99], v[32:33]
	v_exp_f32_e32 v30, v30
	v_pk_mul_f32 v[32:33], v[46:47], v[2:3] op_sel_hi:[0,1]
	v_pk_fma_f32 v[92:93], v[44:45], v[126:127], v[92:93] op_sel_hi:[0,1,1]
	v_exp_f32_e32 v31, v31
	v_pk_fma_f32 v[48:49], v[92:93], v[142:143], v[48:49]
	v_rcp_f32_e32 v55, v55
	v_pk_mul_f32 v[100:101], v[100:101], v[34:35]
	v_exp_f32_e32 v32, v32
	v_pk_mul_f32 v[34:35], v[46:47], v[4:5] op_sel_hi:[0,1]
	v_pk_fma_f32 v[98:99], v[44:45], v[128:129], v[98:99] op_sel_hi:[0,1,1]
	v_exp_f32_e32 v33, v33
	v_pk_fma_f32 v[48:49], v[98:99], v[144:145], v[48:49]
	v_exp_f32_e32 v34, v34
	v_pk_fma_f32 v[100:101], v[44:45], v[130:131], v[100:101] op_sel_hi:[0,1,1]
	v_exp_f32_e32 v35, v35
	v_pk_fma_f32 v[48:49], v[100:101], v[146:147], v[48:49]
	v_add_f32_e32 v54, v48, v49
	v_fma_mix_f32 v54, v87, v182, v54 op_sel:[0,1,0] op_sel_hi:[0,1,0]
	v_mul_f32_e32 v54, v54, v53
	v_fma_mix_f32 v44, v183, v183, 0 op_sel:[0,1,0] op_sel_hi:[1,1,0]
	v_fma_mixlo_f16 v56, v54, v55, 0
	ds_write_b16 v19, v56 offset:1056
	s_waitcnt lgkmcnt(1)
	ds_read_b128 v[116:119], v57 offset:256
	ds_read_b128 v[120:123], v57 offset:272
	ds_read_b128 v[124:127], v57 offset:288
	ds_read_b128 v[128:131], v57 offset:304
	ds_read_b128 v[132:135], v57 offset:4352
	ds_read_b128 v[136:139], v57 offset:4368
	ds_read_b128 v[140:143], v57 offset:4384
	ds_read_b128 v[144:147], v57 offset:4400
	s_waitcnt vmcnt(2)
	v_cvt_f32_f16_e32 v46, v184
	v_cvt_f32_f16_e32 v53, v52
	ds_read_u16 v52, v19 offset:2112
	v_pk_mul_f32 v[94:95], v[94:95], v[20:21]
	v_pk_mul_f32 v[20:21], v[46:47], v[14:15] op_sel_hi:[0,1]
	v_mul_f32_e32 v55, 0xbfb8aa3b, v53
	v_pk_mul_f32 v[102:103], v[102:103], v[22:23]
	v_exp_f32_e32 v20, v20
	v_pk_mul_f32 v[22:23], v[46:47], v[16:17] op_sel_hi:[0,1]
	v_pk_fma_f32 v[94:95], v[44:45], v[196:197], v[94:95] op_sel_hi:[0,1,1]
	v_exp_f32_e32 v21, v21
	v_pk_mul_f32 v[48:49], v[94:95], v[212:213]
	v_pk_mul_f32 v[88:89], v[88:89], v[24:25]
	v_exp_f32_e32 v22, v22
	v_pk_mul_f32 v[24:25], v[46:47], v[10:11] op_sel_hi:[0,1]
	v_pk_fma_f32 v[102:103], v[44:45], v[198:199], v[102:103] op_sel_hi:[0,1,1]
	v_exp_f32_e32 v23, v23
	v_pk_fma_f32 v[48:49], v[102:103], v[214:215], v[48:49]
	v_exp_f32_e32 v55, v55
	v_pk_mul_f32 v[96:97], v[96:97], v[26:27]
	v_exp_f32_e32 v24, v24
	v_pk_mul_f32 v[26:27], v[46:47], v[12:13] op_sel_hi:[0,1]
	v_pk_fma_f32 v[88:89], v[44:45], v[200:201], v[88:89] op_sel_hi:[0,1,1]
	v_exp_f32_e32 v25, v25
	v_pk_fma_f32 v[48:49], v[88:89], v[216:217], v[48:49]
	v_pk_mul_f32 v[90:91], v[90:91], v[28:29]
	v_exp_f32_e32 v26, v26
	v_pk_mul_f32 v[28:29], v[46:47], v[6:7] op_sel_hi:[0,1]
	v_pk_fma_f32 v[96:97], v[44:45], v[202:203], v[96:97] op_sel_hi:[0,1,1]
	v_exp_f32_e32 v27, v27
	v_pk_fma_f32 v[48:49], v[96:97], v[218:219], v[48:49]
	v_add_f32_e32 v55, 1.0, v55
	v_pk_mul_f32 v[92:93], v[92:93], v[30:31]
	v_exp_f32_e32 v28, v28
	v_pk_mul_f32 v[30:31], v[46:47], v[8:9] op_sel_hi:[0,1]
	v_pk_fma_f32 v[90:91], v[44:45], v[204:205], v[90:91] op_sel_hi:[0,1,1]
	v_exp_f32_e32 v29, v29
	v_pk_fma_f32 v[48:49], v[90:91], v[220:221], v[48:49]
	v_pk_mul_f32 v[98:99], v[98:99], v[32:33]
	v_exp_f32_e32 v30, v30
	v_pk_mul_f32 v[32:33], v[46:47], v[2:3] op_sel_hi:[0,1]
	v_pk_fma_f32 v[92:93], v[44:45], v[206:207], v[92:93] op_sel_hi:[0,1,1]
	v_exp_f32_e32 v31, v31
	v_pk_fma_f32 v[48:49], v[92:93], v[222:223], v[48:49]
	v_rcp_f32_e32 v55, v55
	v_pk_mul_f32 v[100:101], v[100:101], v[34:35]
	v_exp_f32_e32 v32, v32
	v_pk_mul_f32 v[34:35], v[46:47], v[4:5] op_sel_hi:[0,1]
	v_pk_fma_f32 v[98:99], v[44:45], v[208:209], v[98:99] op_sel_hi:[0,1,1]
	v_exp_f32_e32 v33, v33
	v_pk_fma_f32 v[48:49], v[98:99], v[224:225], v[48:49]
	v_exp_f32_e32 v34, v34
	v_pk_fma_f32 v[100:101], v[44:45], v[210:211], v[100:101] op_sel_hi:[0,1,1]
	v_exp_f32_e32 v35, v35
	v_pk_fma_f32 v[48:49], v[100:101], v[226:227], v[48:49]
	v_add_f32_e32 v54, v48, v49
	v_fma_mix_f32 v54, v87, v183, v54 op_sel:[0,1,0] op_sel_hi:[0,1,0]
	v_mul_f32_e32 v54, v54, v53
	v_fma_mix_f32 v44, v184, v184, 0 op_sel:[0,1,0] op_sel_hi:[1,1,0]
	global_load_dwordx4 v[180:183], v[58:59], off offset:-4096 nt
	v_fma_mixlo_f16 v56, v54, v55, 0
	ds_write_b16 v19, v56 offset:1584
	s_waitcnt lgkmcnt(1)
	ds_read_b128 v[196:199], v57 offset:320
	ds_read_b128 v[200:203], v57 offset:336
	ds_read_b128 v[204:207], v57 offset:352
	ds_read_b128 v[208:211], v57 offset:368
	ds_read_b128 v[212:215], v57 offset:4416
	ds_read_b128 v[216:219], v57 offset:4432
	ds_read_b128 v[220:223], v57 offset:4448
	ds_read_b128 v[224:227], v57 offset:4464
	v_cvt_f32_f16_e32 v46, v185
	v_cvt_f32_f16_e32 v53, v52
	ds_read_u16 v52, v19 offset:2640
	v_pk_mul_f32 v[94:95], v[94:95], v[20:21]
	v_pk_mul_f32 v[20:21], v[46:47], v[14:15] op_sel_hi:[0,1]
	v_mul_f32_e32 v55, 0xbfb8aa3b, v53
	v_pk_mul_f32 v[102:103], v[102:103], v[22:23]
	v_exp_f32_e32 v20, v20
	v_pk_mul_f32 v[22:23], v[46:47], v[16:17] op_sel_hi:[0,1]
	v_pk_fma_f32 v[94:95], v[44:45], v[116:117], v[94:95] op_sel_hi:[0,1,1]
	v_exp_f32_e32 v21, v21
	v_pk_mul_f32 v[48:49], v[94:95], v[132:133]
	v_pk_mul_f32 v[88:89], v[88:89], v[24:25]
	v_exp_f32_e32 v22, v22
	v_pk_mul_f32 v[24:25], v[46:47], v[10:11] op_sel_hi:[0,1]
	v_pk_fma_f32 v[102:103], v[44:45], v[118:119], v[102:103] op_sel_hi:[0,1,1]
	v_exp_f32_e32 v23, v23
	v_pk_fma_f32 v[48:49], v[102:103], v[134:135], v[48:49]
	v_exp_f32_e32 v55, v55
	v_pk_mul_f32 v[96:97], v[96:97], v[26:27]
	v_exp_f32_e32 v24, v24
	v_pk_mul_f32 v[26:27], v[46:47], v[12:13] op_sel_hi:[0,1]
	v_pk_fma_f32 v[88:89], v[44:45], v[120:121], v[88:89] op_sel_hi:[0,1,1]
	v_exp_f32_e32 v25, v25
	v_pk_fma_f32 v[48:49], v[88:89], v[136:137], v[48:49]
	v_pk_mul_f32 v[90:91], v[90:91], v[28:29]
	v_exp_f32_e32 v26, v26
	v_pk_mul_f32 v[28:29], v[46:47], v[6:7] op_sel_hi:[0,1]
	v_pk_fma_f32 v[96:97], v[44:45], v[122:123], v[96:97] op_sel_hi:[0,1,1]
	v_exp_f32_e32 v27, v27
	v_pk_fma_f32 v[48:49], v[96:97], v[138:139], v[48:49]
	v_add_f32_e32 v55, 1.0, v55
	v_pk_mul_f32 v[92:93], v[92:93], v[30:31]
	v_exp_f32_e32 v28, v28
	v_pk_mul_f32 v[30:31], v[46:47], v[8:9] op_sel_hi:[0,1]
	v_pk_fma_f32 v[90:91], v[44:45], v[124:125], v[90:91] op_sel_hi:[0,1,1]
	v_exp_f32_e32 v29, v29
	v_pk_fma_f32 v[48:49], v[90:91], v[140:141], v[48:49]
	v_pk_mul_f32 v[98:99], v[98:99], v[32:33]
	v_exp_f32_e32 v30, v30
	v_pk_mul_f32 v[32:33], v[46:47], v[2:3] op_sel_hi:[0,1]
	v_pk_fma_f32 v[92:93], v[44:45], v[126:127], v[92:93] op_sel_hi:[0,1,1]
	v_exp_f32_e32 v31, v31
	v_pk_fma_f32 v[48:49], v[92:93], v[142:143], v[48:49]
	v_rcp_f32_e32 v55, v55
	v_pk_mul_f32 v[100:101], v[100:101], v[34:35]
	v_exp_f32_e32 v32, v32
	v_pk_mul_f32 v[34:35], v[46:47], v[4:5] op_sel_hi:[0,1]
	v_pk_fma_f32 v[98:99], v[44:45], v[128:129], v[98:99] op_sel_hi:[0,1,1]
	v_exp_f32_e32 v33, v33
	v_pk_fma_f32 v[48:49], v[98:99], v[144:145], v[48:49]
	v_exp_f32_e32 v34, v34
	v_pk_fma_f32 v[100:101], v[44:45], v[130:131], v[100:101] op_sel_hi:[0,1,1]
	v_exp_f32_e32 v35, v35
	v_pk_fma_f32 v[48:49], v[100:101], v[146:147], v[48:49]
	v_add_f32_e32 v54, v48, v49
	v_fma_mix_f32 v54, v87, v184, v54 op_sel:[0,1,0] op_sel_hi:[0,1,0]
	v_mul_f32_e32 v54, v54, v53
	v_fma_mix_f32 v44, v185, v185, 0 op_sel:[0,1,0] op_sel_hi:[1,1,0]
	v_fma_mixlo_f16 v56, v54, v55, 0
	ds_write_b16 v19, v56 offset:2112
	s_waitcnt lgkmcnt(1)
	ds_read_b128 v[116:119], v57 offset:384
	ds_read_b128 v[120:123], v57 offset:400
	ds_read_b128 v[124:127], v57 offset:416
	ds_read_b128 v[128:131], v57 offset:432
	ds_read_b128 v[132:135], v57 offset:4480
	ds_read_b128 v[136:139], v57 offset:4496
	ds_read_b128 v[140:143], v57 offset:4512
	ds_read_b128 v[144:147], v57 offset:4528
	v_cvt_f32_f16_e32 v46, v186
	v_cvt_f32_f16_e32 v53, v52
	ds_read_u16 v52, v19 offset:3168
	v_pk_mul_f32 v[94:95], v[94:95], v[20:21]
	v_pk_mul_f32 v[20:21], v[46:47], v[14:15] op_sel_hi:[0,1]
	v_mul_f32_e32 v55, 0xbfb8aa3b, v53
	v_pk_mul_f32 v[102:103], v[102:103], v[22:23]
	v_exp_f32_e32 v20, v20
	v_pk_mul_f32 v[22:23], v[46:47], v[16:17] op_sel_hi:[0,1]
	v_pk_fma_f32 v[94:95], v[44:45], v[196:197], v[94:95] op_sel_hi:[0,1,1]
	v_exp_f32_e32 v21, v21
	v_pk_mul_f32 v[48:49], v[94:95], v[212:213]
	v_pk_mul_f32 v[88:89], v[88:89], v[24:25]
	v_exp_f32_e32 v22, v22
	v_pk_mul_f32 v[24:25], v[46:47], v[10:11] op_sel_hi:[0,1]
	v_pk_fma_f32 v[102:103], v[44:45], v[198:199], v[102:103] op_sel_hi:[0,1,1]
	v_exp_f32_e32 v23, v23
	v_pk_fma_f32 v[48:49], v[102:103], v[214:215], v[48:49]
	v_exp_f32_e32 v55, v55
	v_pk_mul_f32 v[96:97], v[96:97], v[26:27]
	v_exp_f32_e32 v24, v24
	v_pk_mul_f32 v[26:27], v[46:47], v[12:13] op_sel_hi:[0,1]
	v_pk_fma_f32 v[88:89], v[44:45], v[200:201], v[88:89] op_sel_hi:[0,1,1]
	v_exp_f32_e32 v25, v25
	v_pk_fma_f32 v[48:49], v[88:89], v[216:217], v[48:49]
	v_pk_mul_f32 v[90:91], v[90:91], v[28:29]
	v_exp_f32_e32 v26, v26
	v_pk_mul_f32 v[28:29], v[46:47], v[6:7] op_sel_hi:[0,1]
	v_pk_fma_f32 v[96:97], v[44:45], v[202:203], v[96:97] op_sel_hi:[0,1,1]
	v_exp_f32_e32 v27, v27
	v_pk_fma_f32 v[48:49], v[96:97], v[218:219], v[48:49]
	v_add_f32_e32 v55, 1.0, v55
	v_pk_mul_f32 v[92:93], v[92:93], v[30:31]
	v_exp_f32_e32 v28, v28
	v_pk_mul_f32 v[30:31], v[46:47], v[8:9] op_sel_hi:[0,1]
	v_pk_fma_f32 v[90:91], v[44:45], v[204:205], v[90:91] op_sel_hi:[0,1,1]
	v_exp_f32_e32 v29, v29
	v_pk_fma_f32 v[48:49], v[90:91], v[220:221], v[48:49]
	v_pk_mul_f32 v[98:99], v[98:99], v[32:33]
	v_exp_f32_e32 v30, v30
	v_pk_mul_f32 v[32:33], v[46:47], v[2:3] op_sel_hi:[0,1]
	v_pk_fma_f32 v[92:93], v[44:45], v[206:207], v[92:93] op_sel_hi:[0,1,1]
	v_exp_f32_e32 v31, v31
	v_pk_fma_f32 v[48:49], v[92:93], v[222:223], v[48:49]
	v_rcp_f32_e32 v55, v55
	v_pk_mul_f32 v[100:101], v[100:101], v[34:35]
	v_exp_f32_e32 v32, v32
	v_pk_mul_f32 v[34:35], v[46:47], v[4:5] op_sel_hi:[0,1]
	v_pk_fma_f32 v[98:99], v[44:45], v[208:209], v[98:99] op_sel_hi:[0,1,1]
	v_exp_f32_e32 v33, v33
	v_pk_fma_f32 v[48:49], v[98:99], v[224:225], v[48:49]
	v_exp_f32_e32 v34, v34
	v_pk_fma_f32 v[100:101], v[44:45], v[210:211], v[100:101] op_sel_hi:[0,1,1]
	v_exp_f32_e32 v35, v35
	v_pk_fma_f32 v[48:49], v[100:101], v[226:227], v[48:49]
	v_add_f32_e32 v54, v48, v49
	v_fma_mix_f32 v54, v87, v185, v54 op_sel:[0,1,0] op_sel_hi:[0,1,0]
	v_mul_f32_e32 v54, v54, v53
	v_fma_mix_f32 v44, v186, v186, 0 op_sel:[0,1,0] op_sel_hi:[1,1,0]
	v_fma_mixlo_f16 v56, v54, v55, 0
	ds_write_b16 v19, v56 offset:2640
	s_waitcnt lgkmcnt(1)
	ds_read_b128 v[196:199], v57 offset:448
	ds_read_b128 v[200:203], v57 offset:464
	ds_read_b128 v[204:207], v57 offset:480
	ds_read_b128 v[208:211], v57 offset:496
	ds_read_b128 v[212:215], v57 offset:4544
	ds_read_b128 v[216:219], v57 offset:4560
	ds_read_b128 v[220:223], v57 offset:4576
	ds_read_b128 v[224:227], v57 offset:4592
	v_cvt_f32_f16_e32 v46, v187
	v_cvt_f32_f16_e32 v53, v52
	ds_read_u16 v52, v19 offset:3696
	v_pk_mul_f32 v[94:95], v[94:95], v[20:21]
	v_pk_mul_f32 v[20:21], v[46:47], v[14:15] op_sel_hi:[0,1]
	v_mul_f32_e32 v55, 0xbfb8aa3b, v53
	v_pk_mul_f32 v[102:103], v[102:103], v[22:23]
	v_exp_f32_e32 v20, v20
	v_pk_mul_f32 v[22:23], v[46:47], v[16:17] op_sel_hi:[0,1]
	v_pk_fma_f32 v[94:95], v[44:45], v[116:117], v[94:95] op_sel_hi:[0,1,1]
	v_exp_f32_e32 v21, v21
	v_pk_mul_f32 v[48:49], v[94:95], v[132:133]
	v_pk_mul_f32 v[88:89], v[88:89], v[24:25]
	v_exp_f32_e32 v22, v22
	v_pk_mul_f32 v[24:25], v[46:47], v[10:11] op_sel_hi:[0,1]
	v_pk_fma_f32 v[102:103], v[44:45], v[118:119], v[102:103] op_sel_hi:[0,1,1]
	v_exp_f32_e32 v23, v23
	v_pk_fma_f32 v[48:49], v[102:103], v[134:135], v[48:49]
	v_exp_f32_e32 v55, v55
	v_pk_mul_f32 v[96:97], v[96:97], v[26:27]
	v_exp_f32_e32 v24, v24
	v_pk_mul_f32 v[26:27], v[46:47], v[12:13] op_sel_hi:[0,1]
	v_pk_fma_f32 v[88:89], v[44:45], v[120:121], v[88:89] op_sel_hi:[0,1,1]
	v_exp_f32_e32 v25, v25
	v_pk_fma_f32 v[48:49], v[88:89], v[136:137], v[48:49]
	v_pk_mul_f32 v[90:91], v[90:91], v[28:29]
	v_exp_f32_e32 v26, v26
	v_pk_mul_f32 v[28:29], v[46:47], v[6:7] op_sel_hi:[0,1]
	v_pk_fma_f32 v[96:97], v[44:45], v[122:123], v[96:97] op_sel_hi:[0,1,1]
	v_exp_f32_e32 v27, v27
	v_pk_fma_f32 v[48:49], v[96:97], v[138:139], v[48:49]
	v_add_f32_e32 v55, 1.0, v55
	v_pk_mul_f32 v[92:93], v[92:93], v[30:31]
	v_exp_f32_e32 v28, v28
	v_pk_mul_f32 v[30:31], v[46:47], v[8:9] op_sel_hi:[0,1]
	v_pk_fma_f32 v[90:91], v[44:45], v[124:125], v[90:91] op_sel_hi:[0,1,1]
	v_exp_f32_e32 v29, v29
	v_pk_fma_f32 v[48:49], v[90:91], v[140:141], v[48:49]
	v_pk_mul_f32 v[98:99], v[98:99], v[32:33]
	v_exp_f32_e32 v30, v30
	v_pk_mul_f32 v[32:33], v[46:47], v[2:3] op_sel_hi:[0,1]
	v_pk_fma_f32 v[92:93], v[44:45], v[126:127], v[92:93] op_sel_hi:[0,1,1]
	v_exp_f32_e32 v31, v31
	v_pk_fma_f32 v[48:49], v[92:93], v[142:143], v[48:49]
	v_rcp_f32_e32 v55, v55
	v_pk_mul_f32 v[100:101], v[100:101], v[34:35]
	v_exp_f32_e32 v32, v32
	v_pk_mul_f32 v[34:35], v[46:47], v[4:5] op_sel_hi:[0,1]
	v_pk_fma_f32 v[98:99], v[44:45], v[128:129], v[98:99] op_sel_hi:[0,1,1]
	v_exp_f32_e32 v33, v33
	v_pk_fma_f32 v[48:49], v[98:99], v[144:145], v[48:49]
	v_exp_f32_e32 v34, v34
	v_pk_fma_f32 v[100:101], v[44:45], v[130:131], v[100:101] op_sel_hi:[0,1,1]
	v_exp_f32_e32 v35, v35
	v_pk_fma_f32 v[48:49], v[100:101], v[146:147], v[48:49]
	v_add_f32_e32 v54, v48, v49
	v_fma_mix_f32 v54, v87, v186, v54 op_sel:[0,1,0] op_sel_hi:[0,1,0]
	v_mul_f32_e32 v54, v54, v53
	v_fma_mix_f32 v44, v187, v187, 0 op_sel:[0,1,0] op_sel_hi:[1,1,0]
	v_fma_mixlo_f16 v56, v54, v55, 0
	ds_write_b16 v19, v56 offset:3168
	s_waitcnt lgkmcnt(1)
	ds_read_b128 v[116:119], v57 offset:512
	ds_read_b128 v[120:123], v57 offset:528
	ds_read_b128 v[124:127], v57 offset:544
	ds_read_b128 v[128:131], v57 offset:560
	ds_read_b128 v[132:135], v57 offset:4608
	ds_read_b128 v[136:139], v57 offset:4624
	ds_read_b128 v[140:143], v57 offset:4640
	ds_read_b128 v[144:147], v57 offset:4656
	s_waitcnt vmcnt(2)
	v_cvt_f32_f16_e32 v46, v188
	v_cvt_f32_f16_e32 v53, v52
	ds_read_u16 v52, v19 offset:4224
	v_pk_mul_f32 v[94:95], v[94:95], v[20:21]
	v_pk_mul_f32 v[20:21], v[46:47], v[14:15] op_sel_hi:[0,1]
	v_mul_f32_e32 v55, 0xbfb8aa3b, v53
	v_pk_mul_f32 v[102:103], v[102:103], v[22:23]
	v_exp_f32_e32 v20, v20
	v_pk_mul_f32 v[22:23], v[46:47], v[16:17] op_sel_hi:[0,1]
	v_pk_fma_f32 v[94:95], v[44:45], v[196:197], v[94:95] op_sel_hi:[0,1,1]
	v_exp_f32_e32 v21, v21
	v_pk_mul_f32 v[48:49], v[94:95], v[212:213]
	v_pk_mul_f32 v[88:89], v[88:89], v[24:25]
	v_exp_f32_e32 v22, v22
	v_pk_mul_f32 v[24:25], v[46:47], v[10:11] op_sel_hi:[0,1]
	v_pk_fma_f32 v[102:103], v[44:45], v[198:199], v[102:103] op_sel_hi:[0,1,1]
	v_exp_f32_e32 v23, v23
	v_pk_fma_f32 v[48:49], v[102:103], v[214:215], v[48:49]
	v_exp_f32_e32 v55, v55
	v_pk_mul_f32 v[96:97], v[96:97], v[26:27]
	v_exp_f32_e32 v24, v24
	v_pk_mul_f32 v[26:27], v[46:47], v[12:13] op_sel_hi:[0,1]
	v_pk_fma_f32 v[88:89], v[44:45], v[200:201], v[88:89] op_sel_hi:[0,1,1]
	v_exp_f32_e32 v25, v25
	v_pk_fma_f32 v[48:49], v[88:89], v[216:217], v[48:49]
	v_pk_mul_f32 v[90:91], v[90:91], v[28:29]
	v_exp_f32_e32 v26, v26
	v_pk_mul_f32 v[28:29], v[46:47], v[6:7] op_sel_hi:[0,1]
	v_pk_fma_f32 v[96:97], v[44:45], v[202:203], v[96:97] op_sel_hi:[0,1,1]
	v_exp_f32_e32 v27, v27
	v_pk_fma_f32 v[48:49], v[96:97], v[218:219], v[48:49]
	v_add_f32_e32 v55, 1.0, v55
	v_pk_mul_f32 v[92:93], v[92:93], v[30:31]
	v_exp_f32_e32 v28, v28
	v_pk_mul_f32 v[30:31], v[46:47], v[8:9] op_sel_hi:[0,1]
	v_pk_fma_f32 v[90:91], v[44:45], v[204:205], v[90:91] op_sel_hi:[0,1,1]
	v_exp_f32_e32 v29, v29
	v_pk_fma_f32 v[48:49], v[90:91], v[220:221], v[48:49]
	v_pk_mul_f32 v[98:99], v[98:99], v[32:33]
	v_exp_f32_e32 v30, v30
	v_pk_mul_f32 v[32:33], v[46:47], v[2:3] op_sel_hi:[0,1]
	v_pk_fma_f32 v[92:93], v[44:45], v[206:207], v[92:93] op_sel_hi:[0,1,1]
	v_exp_f32_e32 v31, v31
	v_pk_fma_f32 v[48:49], v[92:93], v[222:223], v[48:49]
	v_rcp_f32_e32 v55, v55
	v_pk_mul_f32 v[100:101], v[100:101], v[34:35]
	v_exp_f32_e32 v32, v32
	v_pk_mul_f32 v[34:35], v[46:47], v[4:5] op_sel_hi:[0,1]
	v_pk_fma_f32 v[98:99], v[44:45], v[208:209], v[98:99] op_sel_hi:[0,1,1]
	v_exp_f32_e32 v33, v33
	v_pk_fma_f32 v[48:49], v[98:99], v[224:225], v[48:49]
	v_exp_f32_e32 v34, v34
	v_pk_fma_f32 v[100:101], v[44:45], v[210:211], v[100:101] op_sel_hi:[0,1,1]
	v_exp_f32_e32 v35, v35
	v_pk_fma_f32 v[48:49], v[100:101], v[226:227], v[48:49]
	v_add_f32_e32 v54, v48, v49
	v_fma_mix_f32 v54, v87, v187, v54 op_sel:[0,1,0] op_sel_hi:[0,1,0]
	v_mul_f32_e32 v54, v54, v53
	v_fma_mix_f32 v44, v188, v188, 0 op_sel:[0,1,0] op_sel_hi:[1,1,0]
	global_load_dwordx4 v[184:187], v[58:59], off nt
	v_fma_mixlo_f16 v56, v54, v55, 0
	ds_write_b16 v19, v56 offset:3696
	s_waitcnt lgkmcnt(1)
	ds_read_b128 v[196:199], v57 offset:576
	ds_read_b128 v[200:203], v57 offset:592
	ds_read_b128 v[204:207], v57 offset:608
	ds_read_b128 v[208:211], v57 offset:624
	ds_read_b128 v[212:215], v57 offset:4672
	ds_read_b128 v[216:219], v57 offset:4688
	ds_read_b128 v[220:223], v57 offset:4704
	ds_read_b128 v[224:227], v57 offset:4720
	v_cvt_f32_f16_e32 v46, v189
	v_cvt_f32_f16_e32 v53, v52
	ds_read_u16 v52, v19 offset:4752
	v_pk_mul_f32 v[94:95], v[94:95], v[20:21]
	v_pk_mul_f32 v[20:21], v[46:47], v[14:15] op_sel_hi:[0,1]
	v_mul_f32_e32 v55, 0xbfb8aa3b, v53
	v_pk_mul_f32 v[102:103], v[102:103], v[22:23]
	v_exp_f32_e32 v20, v20
	v_pk_mul_f32 v[22:23], v[46:47], v[16:17] op_sel_hi:[0,1]
	v_pk_fma_f32 v[94:95], v[44:45], v[116:117], v[94:95] op_sel_hi:[0,1,1]
	v_exp_f32_e32 v21, v21
	v_pk_mul_f32 v[48:49], v[94:95], v[132:133]
	v_pk_mul_f32 v[88:89], v[88:89], v[24:25]
	v_exp_f32_e32 v22, v22
	v_pk_mul_f32 v[24:25], v[46:47], v[10:11] op_sel_hi:[0,1]
	v_pk_fma_f32 v[102:103], v[44:45], v[118:119], v[102:103] op_sel_hi:[0,1,1]
	v_exp_f32_e32 v23, v23
	v_pk_fma_f32 v[48:49], v[102:103], v[134:135], v[48:49]
	v_exp_f32_e32 v55, v55
	v_pk_mul_f32 v[96:97], v[96:97], v[26:27]
	v_exp_f32_e32 v24, v24
	v_pk_mul_f32 v[26:27], v[46:47], v[12:13] op_sel_hi:[0,1]
	v_pk_fma_f32 v[88:89], v[44:45], v[120:121], v[88:89] op_sel_hi:[0,1,1]
	v_exp_f32_e32 v25, v25
	v_pk_fma_f32 v[48:49], v[88:89], v[136:137], v[48:49]
	v_pk_mul_f32 v[90:91], v[90:91], v[28:29]
	v_exp_f32_e32 v26, v26
	v_pk_mul_f32 v[28:29], v[46:47], v[6:7] op_sel_hi:[0,1]
	v_pk_fma_f32 v[96:97], v[44:45], v[122:123], v[96:97] op_sel_hi:[0,1,1]
	v_exp_f32_e32 v27, v27
	v_pk_fma_f32 v[48:49], v[96:97], v[138:139], v[48:49]
	v_add_f32_e32 v55, 1.0, v55
	v_pk_mul_f32 v[92:93], v[92:93], v[30:31]
	v_exp_f32_e32 v28, v28
	v_pk_mul_f32 v[30:31], v[46:47], v[8:9] op_sel_hi:[0,1]
	v_pk_fma_f32 v[90:91], v[44:45], v[124:125], v[90:91] op_sel_hi:[0,1,1]
	v_exp_f32_e32 v29, v29
	v_pk_fma_f32 v[48:49], v[90:91], v[140:141], v[48:49]
	v_pk_mul_f32 v[98:99], v[98:99], v[32:33]
	v_exp_f32_e32 v30, v30
	v_pk_mul_f32 v[32:33], v[46:47], v[2:3] op_sel_hi:[0,1]
	v_pk_fma_f32 v[92:93], v[44:45], v[126:127], v[92:93] op_sel_hi:[0,1,1]
	v_exp_f32_e32 v31, v31
	v_pk_fma_f32 v[48:49], v[92:93], v[142:143], v[48:49]
	v_rcp_f32_e32 v55, v55
	v_pk_mul_f32 v[100:101], v[100:101], v[34:35]
	v_exp_f32_e32 v32, v32
	v_pk_mul_f32 v[34:35], v[46:47], v[4:5] op_sel_hi:[0,1]
	v_pk_fma_f32 v[98:99], v[44:45], v[128:129], v[98:99] op_sel_hi:[0,1,1]
	v_exp_f32_e32 v33, v33
	v_pk_fma_f32 v[48:49], v[98:99], v[144:145], v[48:49]
	v_exp_f32_e32 v34, v34
	v_pk_fma_f32 v[100:101], v[44:45], v[130:131], v[100:101] op_sel_hi:[0,1,1]
	v_exp_f32_e32 v35, v35
	v_pk_fma_f32 v[48:49], v[100:101], v[146:147], v[48:49]
	v_add_f32_e32 v54, v48, v49
	v_fma_mix_f32 v54, v87, v188, v54 op_sel:[0,1,0] op_sel_hi:[0,1,0]
	v_mul_f32_e32 v54, v54, v53
	v_fma_mix_f32 v44, v189, v189, 0 op_sel:[0,1,0] op_sel_hi:[1,1,0]
	v_fma_mixlo_f16 v56, v54, v55, 0
	ds_write_b16 v19, v56 offset:4224
	s_waitcnt lgkmcnt(1)
	ds_read_b128 v[116:119], v57 offset:640
	ds_read_b128 v[120:123], v57 offset:656
	ds_read_b128 v[124:127], v57 offset:672
	ds_read_b128 v[128:131], v57 offset:688
	ds_read_b128 v[132:135], v57 offset:4736
	ds_read_b128 v[136:139], v57 offset:4752
	ds_read_b128 v[140:143], v57 offset:4768
	ds_read_b128 v[144:147], v57 offset:4784
	v_cvt_f32_f16_e32 v46, v190
	v_cvt_f32_f16_e32 v53, v52
	ds_read_u16 v52, v19 offset:5280
	v_pk_mul_f32 v[94:95], v[94:95], v[20:21]
	v_pk_mul_f32 v[20:21], v[46:47], v[14:15] op_sel_hi:[0,1]
	v_mul_f32_e32 v55, 0xbfb8aa3b, v53
	v_pk_mul_f32 v[102:103], v[102:103], v[22:23]
	v_exp_f32_e32 v20, v20
	v_pk_mul_f32 v[22:23], v[46:47], v[16:17] op_sel_hi:[0,1]
	v_pk_fma_f32 v[94:95], v[44:45], v[196:197], v[94:95] op_sel_hi:[0,1,1]
	v_exp_f32_e32 v21, v21
	v_pk_mul_f32 v[48:49], v[94:95], v[212:213]
	v_pk_mul_f32 v[88:89], v[88:89], v[24:25]
	v_exp_f32_e32 v22, v22
	v_pk_mul_f32 v[24:25], v[46:47], v[10:11] op_sel_hi:[0,1]
	v_pk_fma_f32 v[102:103], v[44:45], v[198:199], v[102:103] op_sel_hi:[0,1,1]
	v_exp_f32_e32 v23, v23
	v_pk_fma_f32 v[48:49], v[102:103], v[214:215], v[48:49]
	v_exp_f32_e32 v55, v55
	v_pk_mul_f32 v[96:97], v[96:97], v[26:27]
	v_exp_f32_e32 v24, v24
	v_pk_mul_f32 v[26:27], v[46:47], v[12:13] op_sel_hi:[0,1]
	v_pk_fma_f32 v[88:89], v[44:45], v[200:201], v[88:89] op_sel_hi:[0,1,1]
	v_exp_f32_e32 v25, v25
	v_pk_fma_f32 v[48:49], v[88:89], v[216:217], v[48:49]
	v_pk_mul_f32 v[90:91], v[90:91], v[28:29]
	v_exp_f32_e32 v26, v26
	v_pk_mul_f32 v[28:29], v[46:47], v[6:7] op_sel_hi:[0,1]
	v_pk_fma_f32 v[96:97], v[44:45], v[202:203], v[96:97] op_sel_hi:[0,1,1]
	v_exp_f32_e32 v27, v27
	v_pk_fma_f32 v[48:49], v[96:97], v[218:219], v[48:49]
	v_add_f32_e32 v55, 1.0, v55
	v_pk_mul_f32 v[92:93], v[92:93], v[30:31]
	v_exp_f32_e32 v28, v28
	v_pk_mul_f32 v[30:31], v[46:47], v[8:9] op_sel_hi:[0,1]
	v_pk_fma_f32 v[90:91], v[44:45], v[204:205], v[90:91] op_sel_hi:[0,1,1]
	v_exp_f32_e32 v29, v29
	v_pk_fma_f32 v[48:49], v[90:91], v[220:221], v[48:49]
	v_pk_mul_f32 v[98:99], v[98:99], v[32:33]
	v_exp_f32_e32 v30, v30
	v_pk_mul_f32 v[32:33], v[46:47], v[2:3] op_sel_hi:[0,1]
	v_pk_fma_f32 v[92:93], v[44:45], v[206:207], v[92:93] op_sel_hi:[0,1,1]
	v_exp_f32_e32 v31, v31
	v_pk_fma_f32 v[48:49], v[92:93], v[222:223], v[48:49]
	v_rcp_f32_e32 v55, v55
	v_pk_mul_f32 v[100:101], v[100:101], v[34:35]
	v_exp_f32_e32 v32, v32
	v_pk_mul_f32 v[34:35], v[46:47], v[4:5] op_sel_hi:[0,1]
	v_pk_fma_f32 v[98:99], v[44:45], v[208:209], v[98:99] op_sel_hi:[0,1,1]
	v_exp_f32_e32 v33, v33
	v_pk_fma_f32 v[48:49], v[98:99], v[224:225], v[48:49]
	v_exp_f32_e32 v34, v34
	v_pk_fma_f32 v[100:101], v[44:45], v[210:211], v[100:101] op_sel_hi:[0,1,1]
	v_exp_f32_e32 v35, v35
	v_pk_fma_f32 v[48:49], v[100:101], v[226:227], v[48:49]
	v_add_f32_e32 v54, v48, v49
	v_fma_mix_f32 v54, v87, v189, v54 op_sel:[0,1,0] op_sel_hi:[0,1,0]
	v_mul_f32_e32 v54, v54, v53
	v_fma_mix_f32 v44, v190, v190, 0 op_sel:[0,1,0] op_sel_hi:[1,1,0]
	v_fma_mixlo_f16 v56, v54, v55, 0
	ds_write_b16 v19, v56 offset:4752
	s_waitcnt lgkmcnt(1)
	ds_read_b128 v[196:199], v57 offset:704
	ds_read_b128 v[200:203], v57 offset:720
	ds_read_b128 v[204:207], v57 offset:736
	ds_read_b128 v[208:211], v57 offset:752
	ds_read_b128 v[212:215], v57 offset:4800
	ds_read_b128 v[216:219], v57 offset:4816
	ds_read_b128 v[220:223], v57 offset:4832
	ds_read_b128 v[224:227], v57 offset:4848
	v_cvt_f32_f16_e32 v46, v191
	v_cvt_f32_f16_e32 v53, v52
	ds_read_u16 v52, v19 offset:5808
	v_pk_mul_f32 v[94:95], v[94:95], v[20:21]
	v_pk_mul_f32 v[20:21], v[46:47], v[14:15] op_sel_hi:[0,1]
	v_mul_f32_e32 v55, 0xbfb8aa3b, v53
	v_pk_mul_f32 v[102:103], v[102:103], v[22:23]
	v_exp_f32_e32 v20, v20
	v_pk_mul_f32 v[22:23], v[46:47], v[16:17] op_sel_hi:[0,1]
	v_pk_fma_f32 v[94:95], v[44:45], v[116:117], v[94:95] op_sel_hi:[0,1,1]
	v_exp_f32_e32 v21, v21
	v_pk_mul_f32 v[48:49], v[94:95], v[132:133]
	v_pk_mul_f32 v[88:89], v[88:89], v[24:25]
	v_exp_f32_e32 v22, v22
	v_pk_mul_f32 v[24:25], v[46:47], v[10:11] op_sel_hi:[0,1]
	v_pk_fma_f32 v[102:103], v[44:45], v[118:119], v[102:103] op_sel_hi:[0,1,1]
	v_exp_f32_e32 v23, v23
	v_pk_fma_f32 v[48:49], v[102:103], v[134:135], v[48:49]
	v_exp_f32_e32 v55, v55
	v_pk_mul_f32 v[96:97], v[96:97], v[26:27]
	v_exp_f32_e32 v24, v24
	v_pk_mul_f32 v[26:27], v[46:47], v[12:13] op_sel_hi:[0,1]
	v_pk_fma_f32 v[88:89], v[44:45], v[120:121], v[88:89] op_sel_hi:[0,1,1]
	v_exp_f32_e32 v25, v25
	v_pk_fma_f32 v[48:49], v[88:89], v[136:137], v[48:49]
	v_pk_mul_f32 v[90:91], v[90:91], v[28:29]
	v_exp_f32_e32 v26, v26
	v_pk_mul_f32 v[28:29], v[46:47], v[6:7] op_sel_hi:[0,1]
	v_pk_fma_f32 v[96:97], v[44:45], v[122:123], v[96:97] op_sel_hi:[0,1,1]
	v_exp_f32_e32 v27, v27
	v_pk_fma_f32 v[48:49], v[96:97], v[138:139], v[48:49]
	v_add_f32_e32 v55, 1.0, v55
	v_pk_mul_f32 v[92:93], v[92:93], v[30:31]
	v_exp_f32_e32 v28, v28
	v_pk_mul_f32 v[30:31], v[46:47], v[8:9] op_sel_hi:[0,1]
	v_pk_fma_f32 v[90:91], v[44:45], v[124:125], v[90:91] op_sel_hi:[0,1,1]
	v_exp_f32_e32 v29, v29
	v_pk_fma_f32 v[48:49], v[90:91], v[140:141], v[48:49]
	v_pk_mul_f32 v[98:99], v[98:99], v[32:33]
	v_exp_f32_e32 v30, v30
	v_pk_mul_f32 v[32:33], v[46:47], v[2:3] op_sel_hi:[0,1]
	v_pk_fma_f32 v[92:93], v[44:45], v[126:127], v[92:93] op_sel_hi:[0,1,1]
	v_exp_f32_e32 v31, v31
	v_pk_fma_f32 v[48:49], v[92:93], v[142:143], v[48:49]
	v_rcp_f32_e32 v55, v55
	v_pk_mul_f32 v[100:101], v[100:101], v[34:35]
	v_exp_f32_e32 v32, v32
	v_pk_mul_f32 v[34:35], v[46:47], v[4:5] op_sel_hi:[0,1]
	v_pk_fma_f32 v[98:99], v[44:45], v[128:129], v[98:99] op_sel_hi:[0,1,1]
	v_exp_f32_e32 v33, v33
	v_pk_fma_f32 v[48:49], v[98:99], v[144:145], v[48:49]
	v_exp_f32_e32 v34, v34
	v_pk_fma_f32 v[100:101], v[44:45], v[130:131], v[100:101] op_sel_hi:[0,1,1]
	v_exp_f32_e32 v35, v35
	v_pk_fma_f32 v[48:49], v[100:101], v[146:147], v[48:49]
	v_add_f32_e32 v54, v48, v49
	v_fma_mix_f32 v54, v87, v190, v54 op_sel:[0,1,0] op_sel_hi:[0,1,0]
	v_mul_f32_e32 v54, v54, v53
	v_fma_mix_f32 v44, v191, v191, 0 op_sel:[0,1,0] op_sel_hi:[1,1,0]
	v_fma_mixlo_f16 v56, v54, v55, 0
	ds_write_b16 v19, v56 offset:5280
	s_waitcnt lgkmcnt(1)
	ds_read_b128 v[116:119], v57 offset:768
	ds_read_b128 v[120:123], v57 offset:784
	ds_read_b128 v[124:127], v57 offset:800
	ds_read_b128 v[128:131], v57 offset:816
	ds_read_b128 v[132:135], v57 offset:4864
	ds_read_b128 v[136:139], v57 offset:4880
	ds_read_b128 v[140:143], v57 offset:4896
	ds_read_b128 v[144:147], v57 offset:4912
	s_waitcnt vmcnt(2)
	v_cvt_f32_f16_e32 v46, v192
	v_cvt_f32_f16_e32 v53, v52
	ds_read_u16 v52, v19 offset:6336
	v_pk_mul_f32 v[94:95], v[94:95], v[20:21]
	v_pk_mul_f32 v[20:21], v[46:47], v[14:15] op_sel_hi:[0,1]
	v_mul_f32_e32 v55, 0xbfb8aa3b, v53
	v_pk_mul_f32 v[102:103], v[102:103], v[22:23]
	v_exp_f32_e32 v20, v20
	v_pk_mul_f32 v[22:23], v[46:47], v[16:17] op_sel_hi:[0,1]
	v_pk_fma_f32 v[94:95], v[44:45], v[196:197], v[94:95] op_sel_hi:[0,1,1]
	v_exp_f32_e32 v21, v21
	v_pk_mul_f32 v[48:49], v[94:95], v[212:213]
	v_pk_mul_f32 v[88:89], v[88:89], v[24:25]
	v_exp_f32_e32 v22, v22
	v_pk_mul_f32 v[24:25], v[46:47], v[10:11] op_sel_hi:[0,1]
	v_pk_fma_f32 v[102:103], v[44:45], v[198:199], v[102:103] op_sel_hi:[0,1,1]
	v_exp_f32_e32 v23, v23
	v_pk_fma_f32 v[48:49], v[102:103], v[214:215], v[48:49]
	v_exp_f32_e32 v55, v55
	v_pk_mul_f32 v[96:97], v[96:97], v[26:27]
	v_exp_f32_e32 v24, v24
	v_pk_mul_f32 v[26:27], v[46:47], v[12:13] op_sel_hi:[0,1]
	v_pk_fma_f32 v[88:89], v[44:45], v[200:201], v[88:89] op_sel_hi:[0,1,1]
	v_exp_f32_e32 v25, v25
	v_pk_fma_f32 v[48:49], v[88:89], v[216:217], v[48:49]
	v_pk_mul_f32 v[90:91], v[90:91], v[28:29]
	v_exp_f32_e32 v26, v26
	v_pk_mul_f32 v[28:29], v[46:47], v[6:7] op_sel_hi:[0,1]
	v_pk_fma_f32 v[96:97], v[44:45], v[202:203], v[96:97] op_sel_hi:[0,1,1]
	v_exp_f32_e32 v27, v27
	v_pk_fma_f32 v[48:49], v[96:97], v[218:219], v[48:49]
	v_add_f32_e32 v55, 1.0, v55
	v_pk_mul_f32 v[92:93], v[92:93], v[30:31]
	v_exp_f32_e32 v28, v28
	v_pk_mul_f32 v[30:31], v[46:47], v[8:9] op_sel_hi:[0,1]
	v_pk_fma_f32 v[90:91], v[44:45], v[204:205], v[90:91] op_sel_hi:[0,1,1]
	v_exp_f32_e32 v29, v29
	v_pk_fma_f32 v[48:49], v[90:91], v[220:221], v[48:49]
	v_pk_mul_f32 v[98:99], v[98:99], v[32:33]
	v_exp_f32_e32 v30, v30
	v_pk_mul_f32 v[32:33], v[46:47], v[2:3] op_sel_hi:[0,1]
	v_pk_fma_f32 v[92:93], v[44:45], v[206:207], v[92:93] op_sel_hi:[0,1,1]
	v_exp_f32_e32 v31, v31
	v_pk_fma_f32 v[48:49], v[92:93], v[222:223], v[48:49]
	v_rcp_f32_e32 v55, v55
	v_pk_mul_f32 v[100:101], v[100:101], v[34:35]
	v_exp_f32_e32 v32, v32
	v_pk_mul_f32 v[34:35], v[46:47], v[4:5] op_sel_hi:[0,1]
	v_pk_fma_f32 v[98:99], v[44:45], v[208:209], v[98:99] op_sel_hi:[0,1,1]
	v_exp_f32_e32 v33, v33
	v_pk_fma_f32 v[48:49], v[98:99], v[224:225], v[48:49]
	v_exp_f32_e32 v34, v34
	v_pk_fma_f32 v[100:101], v[44:45], v[210:211], v[100:101] op_sel_hi:[0,1,1]
	v_exp_f32_e32 v35, v35
	v_pk_fma_f32 v[48:49], v[100:101], v[226:227], v[48:49]
	v_add_f32_e32 v54, v48, v49
	v_fma_mix_f32 v54, v87, v191, v54 op_sel:[0,1,0] op_sel_hi:[0,1,0]
	v_mul_f32_e32 v54, v54, v53
	v_fma_mix_f32 v44, v192, v192, 0 op_sel:[0,1,0] op_sel_hi:[1,1,0]
	global_load_dwordx4 v[188:191], v[50:51], off offset:-4096 nt
	v_fma_mixlo_f16 v56, v54, v55, 0
	ds_write_b16 v19, v56 offset:5808
	s_waitcnt lgkmcnt(1)
	ds_read_b128 v[196:199], v57 offset:832
	ds_read_b128 v[200:203], v57 offset:848
	ds_read_b128 v[204:207], v57 offset:864
	ds_read_b128 v[208:211], v57 offset:880
	ds_read_b128 v[212:215], v57 offset:4928
	ds_read_b128 v[216:219], v57 offset:4944
	ds_read_b128 v[220:223], v57 offset:4960
	ds_read_b128 v[224:227], v57 offset:4976
	v_cvt_f32_f16_e32 v46, v193
	v_cvt_f32_f16_e32 v53, v52
	ds_read_u16 v52, v19 offset:6864
	v_pk_mul_f32 v[94:95], v[94:95], v[20:21]
	v_pk_mul_f32 v[20:21], v[46:47], v[14:15] op_sel_hi:[0,1]
	v_mul_f32_e32 v55, 0xbfb8aa3b, v53
	v_pk_mul_f32 v[102:103], v[102:103], v[22:23]
	v_exp_f32_e32 v20, v20
	v_pk_mul_f32 v[22:23], v[46:47], v[16:17] op_sel_hi:[0,1]
	v_pk_fma_f32 v[94:95], v[44:45], v[116:117], v[94:95] op_sel_hi:[0,1,1]
	v_exp_f32_e32 v21, v21
	v_pk_mul_f32 v[48:49], v[94:95], v[132:133]
	v_pk_mul_f32 v[88:89], v[88:89], v[24:25]
	v_exp_f32_e32 v22, v22
	v_pk_mul_f32 v[24:25], v[46:47], v[10:11] op_sel_hi:[0,1]
	v_pk_fma_f32 v[102:103], v[44:45], v[118:119], v[102:103] op_sel_hi:[0,1,1]
	v_exp_f32_e32 v23, v23
	v_pk_fma_f32 v[48:49], v[102:103], v[134:135], v[48:49]
	v_exp_f32_e32 v55, v55
	v_pk_mul_f32 v[96:97], v[96:97], v[26:27]
	v_exp_f32_e32 v24, v24
	v_pk_mul_f32 v[26:27], v[46:47], v[12:13] op_sel_hi:[0,1]
	v_pk_fma_f32 v[88:89], v[44:45], v[120:121], v[88:89] op_sel_hi:[0,1,1]
	v_exp_f32_e32 v25, v25
	v_pk_fma_f32 v[48:49], v[88:89], v[136:137], v[48:49]
	v_pk_mul_f32 v[90:91], v[90:91], v[28:29]
	v_exp_f32_e32 v26, v26
	v_pk_mul_f32 v[28:29], v[46:47], v[6:7] op_sel_hi:[0,1]
	v_pk_fma_f32 v[96:97], v[44:45], v[122:123], v[96:97] op_sel_hi:[0,1,1]
	v_exp_f32_e32 v27, v27
	v_pk_fma_f32 v[48:49], v[96:97], v[138:139], v[48:49]
	v_add_f32_e32 v55, 1.0, v55
	v_pk_mul_f32 v[92:93], v[92:93], v[30:31]
	v_exp_f32_e32 v28, v28
	v_pk_mul_f32 v[30:31], v[46:47], v[8:9] op_sel_hi:[0,1]
	v_pk_fma_f32 v[90:91], v[44:45], v[124:125], v[90:91] op_sel_hi:[0,1,1]
	v_exp_f32_e32 v29, v29
	v_pk_fma_f32 v[48:49], v[90:91], v[140:141], v[48:49]
	v_pk_mul_f32 v[98:99], v[98:99], v[32:33]
	v_exp_f32_e32 v30, v30
	v_pk_mul_f32 v[32:33], v[46:47], v[2:3] op_sel_hi:[0,1]
	v_pk_fma_f32 v[92:93], v[44:45], v[126:127], v[92:93] op_sel_hi:[0,1,1]
	v_exp_f32_e32 v31, v31
	v_pk_fma_f32 v[48:49], v[92:93], v[142:143], v[48:49]
	v_rcp_f32_e32 v55, v55
	v_pk_mul_f32 v[100:101], v[100:101], v[34:35]
	v_exp_f32_e32 v32, v32
	v_pk_mul_f32 v[34:35], v[46:47], v[4:5] op_sel_hi:[0,1]
	v_pk_fma_f32 v[98:99], v[44:45], v[128:129], v[98:99] op_sel_hi:[0,1,1]
	v_exp_f32_e32 v33, v33
	v_pk_fma_f32 v[48:49], v[98:99], v[144:145], v[48:49]
	v_exp_f32_e32 v34, v34
	v_pk_fma_f32 v[100:101], v[44:45], v[130:131], v[100:101] op_sel_hi:[0,1,1]
	v_exp_f32_e32 v35, v35
	v_pk_fma_f32 v[48:49], v[100:101], v[146:147], v[48:49]
	v_add_f32_e32 v54, v48, v49
	v_fma_mix_f32 v54, v87, v192, v54 op_sel:[0,1,0] op_sel_hi:[0,1,0]
	v_mul_f32_e32 v54, v54, v53
	v_fma_mix_f32 v44, v193, v193, 0 op_sel:[0,1,0] op_sel_hi:[1,1,0]
	v_fma_mixlo_f16 v56, v54, v55, 0
	ds_write_b16 v19, v56 offset:6336
	s_waitcnt lgkmcnt(1)
	ds_read_b128 v[116:119], v57 offset:896
	ds_read_b128 v[120:123], v57 offset:912
	ds_read_b128 v[124:127], v57 offset:928
	ds_read_b128 v[128:131], v57 offset:944
	ds_read_b128 v[132:135], v57 offset:4992
	ds_read_b128 v[136:139], v57 offset:5008
	ds_read_b128 v[140:143], v57 offset:5024
	ds_read_b128 v[144:147], v57 offset:5040
	v_cvt_f32_f16_e32 v46, v194
	v_cvt_f32_f16_e32 v53, v52
	ds_read_u16 v52, v19 offset:7392
	v_pk_mul_f32 v[94:95], v[94:95], v[20:21]
	v_pk_mul_f32 v[20:21], v[46:47], v[14:15] op_sel_hi:[0,1]
	v_mul_f32_e32 v55, 0xbfb8aa3b, v53
	v_pk_mul_f32 v[102:103], v[102:103], v[22:23]
	v_exp_f32_e32 v20, v20
	v_pk_mul_f32 v[22:23], v[46:47], v[16:17] op_sel_hi:[0,1]
	v_pk_fma_f32 v[94:95], v[44:45], v[196:197], v[94:95] op_sel_hi:[0,1,1]
	v_exp_f32_e32 v21, v21
	v_pk_mul_f32 v[48:49], v[94:95], v[212:213]
	v_pk_mul_f32 v[88:89], v[88:89], v[24:25]
	v_exp_f32_e32 v22, v22
	v_pk_mul_f32 v[24:25], v[46:47], v[10:11] op_sel_hi:[0,1]
	v_pk_fma_f32 v[102:103], v[44:45], v[198:199], v[102:103] op_sel_hi:[0,1,1]
	v_exp_f32_e32 v23, v23
	v_pk_fma_f32 v[48:49], v[102:103], v[214:215], v[48:49]
	v_exp_f32_e32 v55, v55
	v_pk_mul_f32 v[96:97], v[96:97], v[26:27]
	v_exp_f32_e32 v24, v24
	v_pk_mul_f32 v[26:27], v[46:47], v[12:13] op_sel_hi:[0,1]
	v_pk_fma_f32 v[88:89], v[44:45], v[200:201], v[88:89] op_sel_hi:[0,1,1]
	v_exp_f32_e32 v25, v25
	v_pk_fma_f32 v[48:49], v[88:89], v[216:217], v[48:49]
	v_pk_mul_f32 v[90:91], v[90:91], v[28:29]
	v_exp_f32_e32 v26, v26
	v_pk_mul_f32 v[28:29], v[46:47], v[6:7] op_sel_hi:[0,1]
	v_pk_fma_f32 v[96:97], v[44:45], v[202:203], v[96:97] op_sel_hi:[0,1,1]
	v_exp_f32_e32 v27, v27
	v_pk_fma_f32 v[48:49], v[96:97], v[218:219], v[48:49]
	v_add_f32_e32 v55, 1.0, v55
	v_pk_mul_f32 v[92:93], v[92:93], v[30:31]
	v_exp_f32_e32 v28, v28
	v_pk_mul_f32 v[30:31], v[46:47], v[8:9] op_sel_hi:[0,1]
	v_pk_fma_f32 v[90:91], v[44:45], v[204:205], v[90:91] op_sel_hi:[0,1,1]
	v_exp_f32_e32 v29, v29
	v_pk_fma_f32 v[48:49], v[90:91], v[220:221], v[48:49]
	v_pk_mul_f32 v[98:99], v[98:99], v[32:33]
	v_exp_f32_e32 v30, v30
	v_pk_mul_f32 v[32:33], v[46:47], v[2:3] op_sel_hi:[0,1]
	v_pk_fma_f32 v[92:93], v[44:45], v[206:207], v[92:93] op_sel_hi:[0,1,1]
	v_exp_f32_e32 v31, v31
	v_pk_fma_f32 v[48:49], v[92:93], v[222:223], v[48:49]
	v_rcp_f32_e32 v55, v55
	v_pk_mul_f32 v[100:101], v[100:101], v[34:35]
	v_exp_f32_e32 v32, v32
	v_pk_mul_f32 v[34:35], v[46:47], v[4:5] op_sel_hi:[0,1]
	v_pk_fma_f32 v[98:99], v[44:45], v[208:209], v[98:99] op_sel_hi:[0,1,1]
	v_exp_f32_e32 v33, v33
	v_pk_fma_f32 v[48:49], v[98:99], v[224:225], v[48:49]
	v_exp_f32_e32 v34, v34
	v_pk_fma_f32 v[100:101], v[44:45], v[210:211], v[100:101] op_sel_hi:[0,1,1]
	v_exp_f32_e32 v35, v35
	v_pk_fma_f32 v[48:49], v[100:101], v[226:227], v[48:49]
	v_add_f32_e32 v54, v48, v49
	v_fma_mix_f32 v54, v87, v193, v54 op_sel:[0,1,0] op_sel_hi:[0,1,0]
	v_mul_f32_e32 v54, v54, v53
	v_fma_mix_f32 v44, v194, v194, 0 op_sel:[0,1,0] op_sel_hi:[1,1,0]
	v_fma_mixlo_f16 v56, v54, v55, 0
	ds_write_b16 v19, v56 offset:6864
	s_waitcnt lgkmcnt(1)
	ds_read_b128 v[196:199], v57 offset:960
	ds_read_b128 v[200:203], v57 offset:976
	ds_read_b128 v[204:207], v57 offset:992
	ds_read_b128 v[208:211], v57 offset:1008
	ds_read_b128 v[212:215], v57 offset:5056
	ds_read_b128 v[216:219], v57 offset:5072
	ds_read_b128 v[220:223], v57 offset:5088
	ds_read_b128 v[224:227], v57 offset:5104
	v_cvt_f32_f16_e32 v46, v195
	v_cvt_f32_f16_e32 v53, v52
	ds_read_u16 v52, v19 offset:7920
	v_pk_mul_f32 v[94:95], v[94:95], v[20:21]
	v_pk_mul_f32 v[20:21], v[46:47], v[14:15] op_sel_hi:[0,1]
	v_mul_f32_e32 v55, 0xbfb8aa3b, v53
	v_pk_mul_f32 v[102:103], v[102:103], v[22:23]
	v_exp_f32_e32 v20, v20
	v_pk_mul_f32 v[22:23], v[46:47], v[16:17] op_sel_hi:[0,1]
	v_pk_fma_f32 v[94:95], v[44:45], v[116:117], v[94:95] op_sel_hi:[0,1,1]
	v_exp_f32_e32 v21, v21
	v_pk_mul_f32 v[48:49], v[94:95], v[132:133]
	v_pk_mul_f32 v[88:89], v[88:89], v[24:25]
	v_exp_f32_e32 v22, v22
	v_pk_mul_f32 v[24:25], v[46:47], v[10:11] op_sel_hi:[0,1]
	v_pk_fma_f32 v[102:103], v[44:45], v[118:119], v[102:103] op_sel_hi:[0,1,1]
	v_exp_f32_e32 v23, v23
	v_pk_fma_f32 v[48:49], v[102:103], v[134:135], v[48:49]
	v_exp_f32_e32 v55, v55
	v_pk_mul_f32 v[96:97], v[96:97], v[26:27]
	v_exp_f32_e32 v24, v24
	v_pk_mul_f32 v[26:27], v[46:47], v[12:13] op_sel_hi:[0,1]
	v_pk_fma_f32 v[88:89], v[44:45], v[120:121], v[88:89] op_sel_hi:[0,1,1]
	v_exp_f32_e32 v25, v25
	v_pk_fma_f32 v[48:49], v[88:89], v[136:137], v[48:49]
	v_pk_mul_f32 v[90:91], v[90:91], v[28:29]
	v_exp_f32_e32 v26, v26
	v_pk_mul_f32 v[28:29], v[46:47], v[6:7] op_sel_hi:[0,1]
	v_pk_fma_f32 v[96:97], v[44:45], v[122:123], v[96:97] op_sel_hi:[0,1,1]
	v_exp_f32_e32 v27, v27
	v_pk_fma_f32 v[48:49], v[96:97], v[138:139], v[48:49]
	v_add_f32_e32 v55, 1.0, v55
	v_pk_mul_f32 v[92:93], v[92:93], v[30:31]
	v_exp_f32_e32 v28, v28
	v_pk_mul_f32 v[30:31], v[46:47], v[8:9] op_sel_hi:[0,1]
	v_pk_fma_f32 v[90:91], v[44:45], v[124:125], v[90:91] op_sel_hi:[0,1,1]
	v_exp_f32_e32 v29, v29
	v_pk_fma_f32 v[48:49], v[90:91], v[140:141], v[48:49]
	v_pk_mul_f32 v[98:99], v[98:99], v[32:33]
	v_exp_f32_e32 v30, v30
	v_pk_mul_f32 v[32:33], v[46:47], v[2:3] op_sel_hi:[0,1]
	v_pk_fma_f32 v[92:93], v[44:45], v[126:127], v[92:93] op_sel_hi:[0,1,1]
	v_exp_f32_e32 v31, v31
	v_pk_fma_f32 v[48:49], v[92:93], v[142:143], v[48:49]
	v_rcp_f32_e32 v55, v55
	v_pk_mul_f32 v[100:101], v[100:101], v[34:35]
	v_exp_f32_e32 v32, v32
	v_pk_mul_f32 v[34:35], v[46:47], v[4:5] op_sel_hi:[0,1]
	v_pk_fma_f32 v[98:99], v[44:45], v[128:129], v[98:99] op_sel_hi:[0,1,1]
	v_exp_f32_e32 v33, v33
	v_pk_fma_f32 v[48:49], v[98:99], v[144:145], v[48:49]
	v_exp_f32_e32 v34, v34
	v_pk_fma_f32 v[100:101], v[44:45], v[130:131], v[100:101] op_sel_hi:[0,1,1]
	v_exp_f32_e32 v35, v35
	v_pk_fma_f32 v[48:49], v[100:101], v[146:147], v[48:49]
	v_add_f32_e32 v54, v48, v49
	v_fma_mix_f32 v54, v87, v194, v54 op_sel:[0,1,0] op_sel_hi:[0,1,0]
	v_mul_f32_e32 v54, v54, v53
	v_fma_mix_f32 v44, v195, v195, 0 op_sel:[0,1,0] op_sel_hi:[1,1,0]
	v_fma_mixlo_f16 v56, v54, v55, 0
	ds_write_b16 v19, v56 offset:7392
	s_waitcnt lgkmcnt(1)
	ds_read_b128 v[116:119], v57 offset:1024
	ds_read_b128 v[120:123], v57 offset:1040
	ds_read_b128 v[124:127], v57 offset:1056
	ds_read_b128 v[128:131], v57 offset:1072
	ds_read_b128 v[132:135], v57 offset:5120
	ds_read_b128 v[136:139], v57 offset:5136
	ds_read_b128 v[140:143], v57 offset:5152
	ds_read_b128 v[144:147], v57 offset:5168
	s_waitcnt vmcnt(2)
	v_cvt_f32_f16_e32 v46, v180
	v_cvt_f32_f16_e32 v53, v52
	ds_read_u16 v52, v19 offset:8448
	v_pk_mul_f32 v[94:95], v[94:95], v[20:21]
	v_pk_mul_f32 v[20:21], v[46:47], v[14:15] op_sel_hi:[0,1]
	v_mul_f32_e32 v55, 0xbfb8aa3b, v53
	v_pk_mul_f32 v[102:103], v[102:103], v[22:23]
	v_exp_f32_e32 v20, v20
	v_pk_mul_f32 v[22:23], v[46:47], v[16:17] op_sel_hi:[0,1]
	v_pk_fma_f32 v[94:95], v[44:45], v[196:197], v[94:95] op_sel_hi:[0,1,1]
	v_exp_f32_e32 v21, v21
	v_pk_mul_f32 v[48:49], v[94:95], v[212:213]
	v_pk_mul_f32 v[88:89], v[88:89], v[24:25]
	v_exp_f32_e32 v22, v22
	v_pk_mul_f32 v[24:25], v[46:47], v[10:11] op_sel_hi:[0,1]
	v_pk_fma_f32 v[102:103], v[44:45], v[198:199], v[102:103] op_sel_hi:[0,1,1]
	v_exp_f32_e32 v23, v23
	v_pk_fma_f32 v[48:49], v[102:103], v[214:215], v[48:49]
	v_exp_f32_e32 v55, v55
	v_pk_mul_f32 v[96:97], v[96:97], v[26:27]
	v_exp_f32_e32 v24, v24
	v_pk_mul_f32 v[26:27], v[46:47], v[12:13] op_sel_hi:[0,1]
	v_pk_fma_f32 v[88:89], v[44:45], v[200:201], v[88:89] op_sel_hi:[0,1,1]
	v_exp_f32_e32 v25, v25
	v_pk_fma_f32 v[48:49], v[88:89], v[216:217], v[48:49]
	v_pk_mul_f32 v[90:91], v[90:91], v[28:29]
	v_exp_f32_e32 v26, v26
	v_pk_mul_f32 v[28:29], v[46:47], v[6:7] op_sel_hi:[0,1]
	v_pk_fma_f32 v[96:97], v[44:45], v[202:203], v[96:97] op_sel_hi:[0,1,1]
	v_exp_f32_e32 v27, v27
	v_pk_fma_f32 v[48:49], v[96:97], v[218:219], v[48:49]
	v_add_f32_e32 v55, 1.0, v55
	v_pk_mul_f32 v[92:93], v[92:93], v[30:31]
	v_exp_f32_e32 v28, v28
	v_pk_mul_f32 v[30:31], v[46:47], v[8:9] op_sel_hi:[0,1]
	v_pk_fma_f32 v[90:91], v[44:45], v[204:205], v[90:91] op_sel_hi:[0,1,1]
	v_exp_f32_e32 v29, v29
	v_pk_fma_f32 v[48:49], v[90:91], v[220:221], v[48:49]
	v_pk_mul_f32 v[98:99], v[98:99], v[32:33]
	v_exp_f32_e32 v30, v30
	v_pk_mul_f32 v[32:33], v[46:47], v[2:3] op_sel_hi:[0,1]
	v_pk_fma_f32 v[92:93], v[44:45], v[206:207], v[92:93] op_sel_hi:[0,1,1]
	v_exp_f32_e32 v31, v31
	v_pk_fma_f32 v[48:49], v[92:93], v[222:223], v[48:49]
	v_rcp_f32_e32 v55, v55
	v_pk_mul_f32 v[100:101], v[100:101], v[34:35]
	v_exp_f32_e32 v32, v32
	v_pk_mul_f32 v[34:35], v[46:47], v[4:5] op_sel_hi:[0,1]
	v_pk_fma_f32 v[98:99], v[44:45], v[208:209], v[98:99] op_sel_hi:[0,1,1]
	v_exp_f32_e32 v33, v33
	v_pk_fma_f32 v[48:49], v[98:99], v[224:225], v[48:49]
	v_exp_f32_e32 v34, v34
	v_pk_fma_f32 v[100:101], v[44:45], v[210:211], v[100:101] op_sel_hi:[0,1,1]
	v_exp_f32_e32 v35, v35
	v_pk_fma_f32 v[48:49], v[100:101], v[226:227], v[48:49]
	v_add_f32_e32 v54, v48, v49
	v_fma_mix_f32 v54, v87, v195, v54 op_sel:[0,1,0] op_sel_hi:[0,1,0]
	v_mul_f32_e32 v54, v54, v53
	v_fma_mix_f32 v44, v180, v180, 0 op_sel:[0,1,0] op_sel_hi:[1,1,0]
	global_load_dwordx4 v[192:195], v[50:51], off nt
	v_fma_mixlo_f16 v56, v54, v55, 0
	ds_write_b16 v19, v56 offset:7920
	v_add_u32_e32 v19, 0x2100, v19
	v_add_u32_e32 v57, 0x400, v57
	v_lshl_add_u64 v[58:59], v[58:59], 0, s[10:11]
	v_lshl_add_u64 v[50:51], v[50:51], 0, s[10:11]
	s_add_i32 s12, s12, 1
	s_cmp_eq_u32 s12, 4
	s_cbranch_scc0 .Lsc3_loop
	global_load_dwordx4 v[18:21], v86, s[4:5]
	global_load_dwordx4 v[34:37], v86, s[4:5] offset:1024
	global_load_dwordx4 v[38:41], v86, s[4:5] offset:2048
	global_load_dwordx4 v[42:45], v86, s[4:5] offset:3072
	v_mov_b32_e32 v87, 0
	v_and_b32_e32 v112, 31, v0
	v_lshl_add_u64 v[2:3], s[4:5], 0, v[86:87]
	v_and_b32_e32 v5, 8, v114
	v_mul_u32_u24_e32 v6, 0x210, v112
	v_add_co_u32_e32 v4, vcc, 0x1000, v2
	v_lshl_add_u32 v113, v5, 1, v6
	s_nop 0
	v_addc_co_u32_e32 v5, vcc, 0, v3, vcc
	global_load_dwordx4 v[46:49], v[4:5], off
	global_load_dwordx4 v[50:53], v[4:5], off offset:1024
	global_load_dwordx4 v[54:57], v[4:5], off offset:2048
	global_load_dwordx4 v[58:61], v[4:5], off offset:3072
	v_add_co_u32_e32 v6, vcc, 0x2000, v2
	s_movk_i32 s4, 0x110
	s_nop 0
	v_addc_co_u32_e32 v7, vcc, 0, v3, vcc
	global_load_dwordx4 v[62:65], v[6:7], off
	global_load_dwordx4 v[66:69], v[6:7], off offset:1024
	global_load_dwordx4 v[70:73], v[6:7], off offset:2048
	global_load_dwordx4 v[74:77], v[6:7], off offset:3072
	v_add_co_u32_e32 v2, vcc, 0x3000, v2
	s_lshl_b32 s2, s2, 12
	s_nop 0
	v_addc_co_u32_e32 v3, vcc, 0, v3, vcc
	global_load_dwordx4 v[78:81], v[2:3], off
	global_load_dwordx4 v[86:89], v[2:3], off offset:1024
	global_load_dwordx4 v[90:93], v[2:3], off offset:2048
	global_load_dwordx4 v[94:97], v[2:3], off offset:3072
	s_waitcnt lgkmcnt(0)
	s_barrier
	ds_read_b128 v[2:5], v113
	ds_read_b128 v[98:101], v113 offset:32
	ds_read_b128 v[22:25], v113 offset:16896
	ds_read_b128 v[102:105], v113 offset:16928
	s_and_b32 s2, s2, 0xf000
	s_add_u32 s0, s0, s2
	s_addc_u32 s1, s1, 0
	s_add_u32 s2, s6, s26
	s_addc_u32 s3, s7, 0
	v_cmp_eq_u32_e32 vcc, 0, v109
	s_waitcnt vmcnt(15) lgkmcnt(3)
	v_mfma_f32_32x32x16_f16 v[2:17], v[18:21], v[2:5], 0
	s_waitcnt lgkmcnt(1)
	v_mfma_f32_32x32x16_f16 v[18:33], v[18:21], v[22:25], 0
	s_waitcnt vmcnt(14)
	v_mfma_f32_32x32x16_f16 v[2:17], v[34:37], v[98:101], v[2:17]
	s_waitcnt lgkmcnt(0)
	v_mfma_f32_32x32x16_f16 v[18:33], v[34:37], v[102:105], v[18:33]
	ds_read_b128 v[34:37], v113 offset:64
	ds_read_b128 v[98:101], v113 offset:96
	s_waitcnt vmcnt(13) lgkmcnt(1)
	v_mfma_f32_32x32x16_f16 v[2:17], v[38:41], v[34:37], v[2:17]
	ds_read_b128 v[34:37], v113 offset:16960
	ds_read_b128 v[102:105], v113 offset:16992
	s_waitcnt lgkmcnt(1)
	v_mfma_f32_32x32x16_f16 v[18:33], v[38:41], v[34:37], v[18:33]
	ds_read_b128 v[34:37], v113 offset:128
	ds_read_b128 v[38:41], v113 offset:160
	s_waitcnt vmcnt(12)
	v_mfma_f32_32x32x16_f16 v[2:17], v[42:45], v[98:101], v[2:17]
	s_waitcnt lgkmcnt(2)
	v_mfma_f32_32x32x16_f16 v[18:33], v[42:45], v[102:105], v[18:33]
	s_waitcnt vmcnt(11) lgkmcnt(1)
	v_mfma_f32_32x32x16_f16 v[2:17], v[46:49], v[34:37], v[2:17]
	ds_read_b128 v[34:37], v113 offset:17024
	ds_read_b128 v[42:45], v113 offset:17056
	s_waitcnt lgkmcnt(1)
	v_mfma_f32_32x32x16_f16 v[18:33], v[46:49], v[34:37], v[18:33]
	s_waitcnt vmcnt(10)
	v_mfma_f32_32x32x16_f16 v[2:17], v[50:53], v[38:41], v[2:17]
	ds_read_b128 v[34:37], v113 offset:192
	ds_read_b128 v[38:41], v113 offset:224
	s_waitcnt lgkmcnt(2)
	v_mfma_f32_32x32x16_f16 v[18:33], v[50:53], v[42:45], v[18:33]
	s_waitcnt vmcnt(9) lgkmcnt(1)
	v_mfma_f32_32x32x16_f16 v[2:17], v[54:57], v[34:37], v[2:17]
	ds_read_b128 v[34:37], v113 offset:17088
	ds_read_b128 v[42:45], v113 offset:17120
	s_waitcnt lgkmcnt(1)
	v_mfma_f32_32x32x16_f16 v[18:33], v[54:57], v[34:37], v[18:33]
	s_waitcnt vmcnt(8)
	v_mfma_f32_32x32x16_f16 v[2:17], v[58:61], v[38:41], v[2:17]
	ds_read_b128 v[34:37], v113 offset:256
	ds_read_b128 v[38:41], v113 offset:288
	s_waitcnt lgkmcnt(2)
	v_mfma_f32_32x32x16_f16 v[18:33], v[58:61], v[42:45], v[18:33]
	s_waitcnt vmcnt(7) lgkmcnt(1)
	v_mfma_f32_32x32x16_f16 v[2:17], v[62:65], v[34:37], v[2:17]
	ds_read_b128 v[34:37], v113 offset:17152
	ds_read_b128 v[42:45], v113 offset:17184
	s_waitcnt lgkmcnt(1)
	v_mfma_f32_32x32x16_f16 v[18:33], v[62:65], v[34:37], v[18:33]
	s_waitcnt vmcnt(6)
	v_mfma_f32_32x32x16_f16 v[2:17], v[66:69], v[38:41], v[2:17]
	ds_read_b128 v[34:37], v113 offset:320
	ds_read_b128 v[38:41], v113 offset:352
	s_waitcnt lgkmcnt(2)
	v_mfma_f32_32x32x16_f16 v[18:33], v[66:69], v[42:45], v[18:33]
	s_waitcnt vmcnt(5) lgkmcnt(1)
	v_mfma_f32_32x32x16_f16 v[2:17], v[70:73], v[34:37], v[2:17]
	ds_read_b128 v[34:37], v113 offset:17216
	ds_read_b128 v[42:45], v113 offset:17248
	s_waitcnt lgkmcnt(1)
	v_mfma_f32_32x32x16_f16 v[18:33], v[70:73], v[34:37], v[18:33]
	s_waitcnt vmcnt(4)
	v_mfma_f32_32x32x16_f16 v[2:17], v[74:77], v[38:41], v[2:17]
	ds_read_b128 v[34:37], v113 offset:384
	ds_read_b128 v[38:41], v113 offset:416
	s_waitcnt lgkmcnt(2)
	v_mfma_f32_32x32x16_f16 v[18:33], v[74:77], v[42:45], v[18:33]
	s_waitcnt vmcnt(3) lgkmcnt(1)
	v_mfma_f32_32x32x16_f16 v[2:17], v[78:81], v[34:37], v[2:17]
	ds_read_b128 v[34:37], v113 offset:17280
	ds_read_b128 v[42:45], v113 offset:17312
	s_waitcnt lgkmcnt(1)
	v_mfma_f32_32x32x16_f16 v[18:33], v[78:81], v[34:37], v[18:33]
	s_waitcnt vmcnt(2)
	v_mfma_f32_32x32x16_f16 v[2:17], v[86:89], v[38:41], v[2:17]
	ds_read_b128 v[34:37], v113 offset:448
	ds_read_b128 v[38:41], v113 offset:480
	s_waitcnt lgkmcnt(2)
	v_mfma_f32_32x32x16_f16 v[18:33], v[86:89], v[42:45], v[18:33]
	s_waitcnt vmcnt(1) lgkmcnt(1)
	v_mfma_f32_32x32x16_f16 v[2:17], v[90:93], v[34:37], v[2:17]
	ds_read_b128 v[34:37], v113 offset:17344
	ds_read_b128 v[42:45], v113 offset:17376
	s_waitcnt lgkmcnt(0)
	s_barrier
	v_mfma_f32_32x32x16_f16 v[18:33], v[90:93], v[34:37], v[18:33]
	v_lshrrev_b32_e32 v34, 3, v0
	v_and_b32_e32 v34, 4, v34
	v_lshl_or_b32 v34, v107, 5, v34
	v_mul_u32_u24_e32 v34, 0x110, v34
	v_lshl_add_u32 v34, v112, 2, v34
	s_waitcnt vmcnt(0)
	v_mfma_f32_32x32x16_f16 v[2:17], v[94:97], v[38:41], v[2:17]
	v_mfma_f32_32x32x16_f16 v[18:33], v[94:97], v[42:45], v[18:33]
	s_nop 11
	ds_write2_b32 v34, v2, v18 offset1:32
	ds_write2_b32 v34, v3, v19 offset0:68 offset1:100
	ds_write2_b32 v34, v4, v20 offset0:136 offset1:168
	ds_write2_b32 v34, v5, v21 offset0:204 offset1:236
	v_add_u32_e32 v2, 0x800, v34
	ds_write2_b32 v2, v6, v22 offset0:32 offset1:64
	ds_write2_b32 v2, v7, v23 offset0:100 offset1:132
	ds_write2_b32 v2, v8, v24 offset0:168 offset1:200
	v_add_u32_e32 v2, 0xa00, v34
	ds_write2_b32 v2, v9, v25 offset0:108 offset1:140
	v_add_u32_e32 v2, 0x1000, v34
	ds_write2_b32 v2, v10, v26 offset0:64 offset1:96
	ds_write2_b32 v2, v11, v27 offset0:132 offset1:164
	ds_write2_b32 v2, v12, v28 offset0:200 offset1:232
	v_add_u32_e32 v2, 0x1400, v34
	ds_write2_b32 v2, v13, v29 offset0:12 offset1:44
	v_add_u32_e32 v2, 0x1800, v34
	v_and_b32_e32 v5, 60, v84
	v_mov_b32_e32 v8, 0x8800
	ds_write2_b32 v2, v14, v30 offset0:96 offset1:128
	ds_write2_b32 v2, v15, v31 offset0:164 offset1:196
	v_add_u32_e32 v2, 0x1a00, v34
	v_lshlrev_b32_e32 v6, 2, v5
	v_lshl_or_b32 v8, v82, 1, v8
	ds_write2_b32 v2, v16, v32 offset0:104 offset1:136
	v_add_u32_e32 v2, 0x1c00, v34
	v_add_u32_e32 v7, v6, v111
	v_mad_u32_u24 v9, v5, s4, v8
	ds_write2_b32 v2, v17, v33 offset0:44 offset1:76
	s_waitcnt lgkmcnt(0)
	s_barrier
	ds_read_b128 v[10:13], v7
	ds_read_u16 v14, v9
	ds_read_u16 v15, v9 offset:272
	ds_read_u16 v16, v9 offset:544
	ds_read_u16 v9, v9 offset:816
	v_or_b32_e32 v2, s20, v5
	v_mul_u32_u24_e32 v7, 0x110, v5
	s_waitcnt lgkmcnt(3)
	v_cvt_f32_f16_e32 v5, v14
	s_waitcnt lgkmcnt(2)
	v_cvt_f32_f16_e32 v14, v15
	s_waitcnt lgkmcnt(1)
	v_cvt_f32_f16_e32 v15, v16
	s_waitcnt lgkmcnt(0)
	v_cvt_f32_f16_e32 v9, v9
	v_or_b32_e32 v4, s8, v82
	v_ashrrev_i32_e32 v3, 31, v2
	v_add_f32_e32 v16, v10, v5
	v_ashrrev_i32_e32 v5, 31, v4
	v_lshl_add_u64 v[2:3], v[2:3], 1, s[2:3]
	v_add_f32_e32 v14, v11, v14
	v_add_f32_e32 v15, v12, v15
	v_add_f32_e32 v9, v13, v9
	v_lshlrev_b64 v[12:13], 13, v[4:5]
	v_cvt_pk_f16_f32 v11, v15, v9
	v_cvt_pk_f16_f32 v10, v16, v14
	v_lshl_add_u64 v[12:13], v[2:3], 0, v[12:13]
	global_store_dwordx2 v[12:13], v[10:11], off sc1
	v_mul_f32_e32 v11, v14, v14
	v_add_f32_e32 v10, v16, v14
	v_fmac_f32_e32 v11, v16, v16
	v_add_f32_e32 v10, v15, v10
	v_fmac_f32_e32 v11, v15, v15
	v_add_f32_e32 v10, v9, v10
	v_fmac_f32_e32 v11, v9, v9
	s_nop 0
	v_add_f32_dpp v9, v10, v10 quad_perm:[1,0,3,2] row_mask:0xf bank_mask:0xf bound_ctrl:1
	v_add_f32_dpp v11, v11, v11 quad_perm:[1,0,3,2] row_mask:0xf bank_mask:0xf bound_ctrl:1
	s_nop 0
	v_add_f32_dpp v9, v9, v9 quad_perm:[2,3,0,1] row_mask:0xf bank_mask:0xf bound_ctrl:1
	v_add_f32_dpp v11, v11, v11 quad_perm:[2,3,0,1] row_mask:0xf bank_mask:0xf bound_ctrl:1
	s_nop 0
	v_add_f32_dpp v9, v9, v9 row_half_mirror row_mask:0xf bank_mask:0xf bound_ctrl:1
	v_add_f32_dpp v11, v11, v11 row_half_mirror row_mask:0xf bank_mask:0xf bound_ctrl:1
	s_nop 0
	v_mov_b32_dpp v10, v9 row_mirror row_mask:0xf bank_mask:0xf bound_ctrl:1
	v_mov_b32_dpp v12, v11 row_mirror row_mask:0xf bank_mask:0xf bound_ctrl:1
	s_and_saveexec_b64 s[2:3], vcc
	s_cbranch_execz .LBB3_4
	v_lshl_add_u64 v[4:5], v[4:5], 2, s[0:1]
	v_add_f32_e32 v9, v9, v10
	v_add_f32_e32 v11, v11, v12
	global_atomic_add_f32 v[4:5], v9, off
	global_atomic_add_f32 v[4:5], v11, off offset:2048
